# layer-0 hosted expert-weight conversion loop: converts wait only for their own item's loads (vmcnt(16) when the other item's loads are in flight) instead of a merged vmcnt(0)
# speedup vs baseline: 1.0006x; 1.0006x over previous
; #define GAS __attribute__((address_space(1)))
; __device__ __forceinline__ void conv8_store(const ConvJob& J, int tid, const f32x4 (&v)[16]) {
;     const int nblk = J.ncols / 256, k0 = 128 * (J.item / nblk), n0 = J.ncol0 + 256 * (J.item % nblk);
;     const int lane = tid & 63, w = tid >> 6, kg = lane & 7, nq = lane >> 3; const float sc8 = J.sc8;
; #pragma unroll
;     for (int c = 0; c < 4; ++c) { u32x4 o;
; #pragma unroll
;         for (int d = 0; d < 4; ++d) { int wv = __builtin_amdgcn_cvt_pk_fp8_f32(v[4 * d][c] * sc8, v[4 * d + 1][c] * sc8, 0, false);
;             wv = __builtin_amdgcn_cvt_pk_fp8_f32(v[4 * d + 2][c] * sc8, v[4 * d + 3][c] * sc8, wv, true); o[d] = (unsigned)wv; }
;         *(GAS u32x4*)(J.WT + (size_t)conv_dst_row(J.mode, n0 - J.ncol0 + 32 * w + 4 * nq + c) * J.K + k0 + 16 * kg) = o; }
;     ...
;             for (;;) {
;                 const int q1 = q + F.G; const bool m1 = q1 < q_hi;
;                 if (m1) conv8_load(decode(q1 < I_IN ? q1 : q1 + NB16), tid, vb);
;                 conv8_store(decode(q < I_IN ? q : q + NB16), tid, va);
;                 if (!m1) break;
;                 const int q2 = q1 + F.G; const bool m2 = q2 < q_hi;
;                 if (m2) conv8_load(decode(q2 < I_IN ? q2 : q2 + NB16), tid, va);
;                 conv8_store(decode(q1 < I_IN ? q1 : q1 + NB16), tid, vb);
.LBB0_468:
	s_cmp_lg_u32 s78, 0
	s_cbranch_scc1 .Lcvw_a
	s_waitcnt vmcnt(0)
.Lcvw_a:
	s_waitcnt vmcnt(16)
	v_mul_f32_e32 v141, s25, v2
	v_mul_f32_e32 v143, s25, v6
	v_mov_b32_e32 v142, v163
	v_cvt_pk_fp8_f32 v142, v141, v143
	v_mul_f32_e32 v145, s25, v18
	v_mul_f32_e32 v146, s25, v22
	v_mov_b32_e32 v143, v163
	v_cvt_pk_fp8_f32 v143, v145, v146
	v_mul_f32_e32 v141, s25, v10
	v_mul_f32_e32 v144, s25, v14
	v_cvt_pk_fp8_f32 v142, v141, v144 op_sel:[0,0,1]
	v_mul_f32_e32 v141, s25, v26
	v_mul_f32_e32 v144, s25, v30
	v_cvt_pk_fp8_f32 v143, v141, v144 op_sel:[0,0,1]
	v_mul_f32_e32 v141, s25, v34
	v_mul_f32_e32 v145, s25, v38
	v_mov_b32_e32 v144, v163
	v_cvt_pk_fp8_f32 v144, v141, v145
	v_mul_f32_e32 v147, s25, v62
	v_mul_f32_e32 v148, s25, v70
	v_mov_b32_e32 v145, v163
	v_cvt_pk_fp8_f32 v145, v147, v148
	v_mul_f32_e32 v141, s25, v42
	v_mul_f32_e32 v146, s25, v54
	v_cvt_pk_fp8_f32 v144, v141, v146 op_sel:[0,0,1]
	v_mul_f32_e32 v141, s25, v78
	v_mul_f32_e32 v146, s25, v90
	s_add_i32 s50, s50, s33
	v_cvt_pk_fp8_f32 v145, v141, v146 op_sel:[0,0,1]
	v_ashrrev_i32_e32 v141, 31, v140
	v_mov_b64_e32 v[146:147], s[82:83]
	v_add_u32_e32 v139, s50, v135
	s_lshl_b32 s84, s58, 7
	v_mad_u64_u32 v[146:147], s[50:51], s80, v140, v[146:147]
	v_mul_lo_u32 v140, s81, v140
	v_mul_lo_u32 v141, s80, v141
	s_ashr_i32 s85, s84, 31
	v_add3_u32 v147, v140, v147, v141
	v_lshl_add_u64 v[140:141], v[146:147], 0, s[84:85]
	v_lshl_add_u64 v[140:141], v[140:141], 0, v[130:131]
	global_store_dwordx4 v[140:141], v[142:145], off
	s_cmp_lt_i32 s24, 2
	s_mov_b64 s[86:87], -1
	v_or_b32_e32 v142, 1, v139
	v_subrev_u32_e32 v141, s33, v142
	s_cbranch_scc1 .LBB0_474
	s_cmp_gt_i32 s24, 2
	v_lshlrev_b32_e32 v143, 1, v141
	s_cbranch_scc0 .LBB0_471
	v_and_b32_e32 v140, 0xffffff00, v143
	v_and_b32_e32 v144, 0x7d, v142
	v_or3_b32 v140, v144, v140, s2
	s_mov_b64 s[86:87], 0

; #define GAS __attribute__((address_space(1)))
; __device__ __forceinline__ void conv8_store(const ConvJob& J, int tid, const f32x4 (&v)[16]) {
;     const int nblk = J.ncols / 256, k0 = 128 * (J.item / nblk), n0 = J.ncol0 + 256 * (J.item % nblk);
;     const int lane = tid & 63, w = tid >> 6, kg = lane & 7, nq = lane >> 3; const float sc8 = J.sc8;
; #pragma unroll
;     for (int c = 0; c < 4; ++c) { u32x4 o;
; #pragma unroll
;         for (int d = 0; d < 4; ++d) { int wv = __builtin_amdgcn_cvt_pk_fp8_f32(v[4 * d][c] * sc8, v[4 * d + 1][c] * sc8, 0, false);
;             wv = __builtin_amdgcn_cvt_pk_fp8_f32(v[4 * d + 2][c] * sc8, v[4 * d + 3][c] * sc8, wv, true); o[d] = (unsigned)wv; }
;         *(GAS u32x4*)(J.WT + (size_t)conv_dst_row(J.mode, n0 - J.ncol0 + 32 * w + 4 * nq + c) * J.K + k0 + 16 * kg) = o; }
;     ...
;     auto decode = [&](int it) -> ConvJob {
;         int r = it;
;         if (r < I_IN) return ConvJob{w_in, ws + WS_WIN, D_MODEL, IN_WIDTH, 1, r, 0, IN_WIDTH, 1, 64.f}; r -= I_IN;
;         if (r < I_INF) return ConvJob{w_in, ws + WS_WINF, D_MODEL, IN_WIDTH, 0, r, C_HF, HG_WIDTH, 0, 1.f}; r -= I_INF;
;         if (r < I_HG) return ConvJob{w_hg, ws + WS_WHG, HG_WIDTH, D_MODEL, 0, r, 0, D_MODEL, 0, 1.f}; r -= I_HG;
;         if (r < I_ATT) return ConvJob{w_att, ws + WS_WATT, ATT_OUT, D_MODEL, 0, r, 0, D_MODEL, 0, 1.f}; r -= I_ATT;
;         if (r < I_OUT) return ConvJob{w_out, ws + WS_WOUT, D_MODEL, D_MODEL, 0, r, 0, D_MODEL, 1, 64.f}; r -= I_OUT;
;         const int which = r / (NEXP1 * I_E); r -= which * (NEXP1 * I_E);
;         const int e = r / I_E, ri = r % I_E; const int es = gu8 ? 1 : 2;
;         if (which == 0) return ConvJob{(e < N_EXPERTS) ? w_eg + (size_t)e * D_MODEL * EXPERT_FF : w_sg, ws + (moe8 ? WS_WGU8 : WS_WGU) + (size_t)e * 1024 * D_MODEL * es, D_MODEL, EXPERT_FF, 2, ri, 0, EXPERT_FF, gu8 ? 1 : 0, 64.f};
;         if (which == 1) return ConvJob{(e < N_EXPERTS) ? w_eu + (size_t)e * D_MODEL * EXPERT_FF : w_su, ws + (moe8 ? WS_WGU8 : WS_WGU) + (size_t)e * 1024 * D_MODEL * es, D_MODEL, EXPERT_FF, 3, ri, 0, EXPERT_FF, gu8 ? 1 : 0, 64.f};
;         return ConvJob{(e < N_EXPERTS) ? w_ed + (size_t)e * EXPERT_FF * D_MODEL : w_sd, ws + (moe8 ? WS_WDN8 : WS_WDN) + (size_t)e * D_MODEL * EXPERT_FF, EXPERT_FF, D_MODEL, 0, ri, 0, D_MODEL, 1, 64.f};
.LBB0_498:
	v_mul_f32_e32 v141, s25, v5
	v_mul_f32_e32 v144, s25, v9
	v_mov_b32_e32 v140, v163
	v_cvt_pk_fp8_f32 v140, v141, v144
	v_mul_f32_e32 v144, s25, v21
	v_mul_f32_e32 v145, s25, v25
	v_mov_b32_e32 v141, v163
	v_cvt_pk_fp8_f32 v141, v144, v145
	v_mul_f32_e32 v142, s25, v13
	v_mul_f32_e32 v143, s25, v17
	v_cvt_pk_fp8_f32 v140, v142, v143 op_sel:[0,0,1]
	v_mul_f32_e32 v142, s25, v29
	v_mul_f32_e32 v143, s25, v33
	v_cvt_pk_fp8_f32 v141, v142, v143 op_sel:[0,0,1]
	v_mul_f32_e32 v143, s25, v37
	v_mul_f32_e32 v146, s25, v41
	v_mov_b32_e32 v142, v163
	v_cvt_pk_fp8_f32 v142, v143, v146
	v_mul_f32_e32 v146, s25, v65
	v_mul_f32_e32 v147, s25, v73
	v_mov_b32_e32 v143, v163
	v_cvt_pk_fp8_f32 v143, v146, v147
	v_mul_f32_e32 v144, s25, v45
	v_mul_f32_e32 v145, s25, v57
	v_cvt_pk_fp8_f32 v142, v144, v145 op_sel:[0,0,1]
	v_mul_f32_e32 v144, s25, v81
	v_mul_f32_e32 v145, s25, v93
	v_cvt_pk_fp8_f32 v143, v144, v145 op_sel:[0,0,1]
	v_ashrrev_i32_e32 v146, 31, v139
	v_mov_b64_e32 v[144:145], s[82:83]
	v_mad_u64_u32 v[144:145], s[24:25], s80, v139, v[144:145]
	v_mul_lo_u32 v139, s81, v139
	v_mul_lo_u32 v146, s80, v146
	v_add3_u32 v145, v139, v145, v146
	v_lshl_add_u64 v[144:145], v[144:145], 0, s[84:85]
	v_lshl_add_u64 v[144:145], v[144:145], 0, v[130:131]
	s_andn2_b64 vcc, exec, s[78:79]
	s_mov_b64 s[78:79], -1
	global_store_dwordx4 v[144:145], v[140:143], off
	s_cbranch_vccnz .LBB0_403
	s_mov_b32 s98, 0
	s_add_i32 s1, s64, s1
	s_cmpk_gt_i32 s1, 0x13ff
	s_cbranch_scc1 .LBB0_528
	s_add_i32 s24, s1, 0xa0
	s_cmpk_lt_i32 s1, 0x320
	s_cselect_b32 s1, s1, s24
	s_cmpk_lt_i32 s1, 0x320
	s_cbranch_scc1 .LBB0_513
	s_cmpk_gt_u32 s1, 0x35f
	s_cbranch_scc0 .LBB0_514
	s_cmpk_gt_u32 s1, 0x39f
	s_cbranch_scc0 .LBB0_515
	s_cmpk_gt_u32 s1, 0x3bf
	s_cbranch_scc0 .LBB0_516
	s_cmpk_gt_u32 s1, 0x43f
	s_cbranch_scc0 .LBB0_518
	s_add_i32 s24, s1, 0xfffffbc0
	s_mul_i32 s25, s24, 0xfc1
	s_lshr_b32 s25, s25, 23
	s_mulk_i32 s25, 0x820
	s_sub_i32 s25, s24, s25
	s_bfe_u32 s33, s25, 0xb0005
	s_cmpk_gt_u32 s24, 0x81f
	s_mov_b64 s[82:83], -1
	s_cbranch_scc0 .LBB0_510
	s_add_i32 s24, s1, 0xfffff3a0
	s_and_b32 s50, 0xffff, s25
	s_cmpk_lt_u32 s50, 0x800
	s_cselect_b64 s[80:81], -1, 0
	s_lshl_b32 s72, s33, 20
	s_cmpk_gt_u32 s24, 0x81f
	s_cbranch_scc0 .LBB0_508
	s_lshl_b64 s[50:51], s[72:73], 2
	s_waitcnt lgkmcnt(0)
	s_add_u32 s24, s12, s50
	s_addc_u32 s58, s13, s51
	s_and_b64 s[50:51], s[80:81], exec
	s_cselect_b32 s79, s58, s23
	s_cselect_b32 s78, s24, s22
	s_mov_b64 s[82:83], 0

; #define GAS __attribute__((address_space(1)))
; __device__ __forceinline__ void conv8_load(const ConvJob& J, int tid, f32x4 (&v)[16]) {
;     const int nblk = J.ncols / 256, k0 = 128 * (J.item / nblk), n0 = J.ncol0 + 256 * (J.item % nblk);
;     const int lane = tid & 63, w = tid >> 6, kg = lane & 7, nq = lane >> 3;
;     const GAS float* p = J.W + (size_t)(k0 + 16 * kg) * J.N + n0 + 32 * w + 4 * nq;
; #pragma unroll
;     for (int j = 0; j < 16; ++j) v[j] = *(const GAS f32x4*)(p + (size_t)j * J.N);
; }
;     ...
;             for (;;) {
;                 const int q1 = q + F.G; const bool m1 = q1 < q_hi;
;                 if (m1) conv8_load(decode(q1 < I_IN ? q1 : q1 + NB16), tid, vb);
;                 conv8_store(decode(q < I_IN ? q : q + NB16), tid, va);
;                 if (!m1) break;
;                 const int q2 = q1 + F.G; const bool m2 = q2 < q_hi;
;                 if (m2) conv8_load(decode(q2 < I_IN ? q2 : q2 + NB16), tid, va);
;                 conv8_store(decode(q1 < I_IN ? q1 : q1 + NB16), tid, vb);
;                 if (!m2) break;
;                 q = q2; }
.LBB0_527:
	v_cvt_f32_u32_e32 v2, s24
	s_sub_i32 s51, 0, s24
	s_abs_i32 s50, s1
	s_ashr_i32 s25, s1, 31
	v_rcp_iflag_f32_e32 v2, v2
	v_lshlrev_b32_e32 v162, 2, v134
	v_mul_f32_e32 v2, 0x4f7ffffe, v2
	v_cvt_u32_f32_e32 v2, v2
	s_nop 0
	v_readfirstlane_b32 s58, v2
	s_mul_i32 s51, s51, s58
	s_mul_hi_u32 s51, s58, s51
	s_add_i32 s58, s58, s51
	s_mul_hi_u32 s51, s50, s58
	s_mul_i32 s58, s51, s24
	s_sub_i32 s50, s50, s58
	s_add_i32 s59, s51, 1
	s_sub_i32 s58, s50, s24
	s_cmp_ge_u32 s50, s24
	s_cselect_b32 s51, s59, s51
	s_cselect_b32 s50, s58, s50
	s_add_i32 s58, s51, 1
	s_cmp_ge_u32 s50, s24
	s_cselect_b32 s50, s58, s51
	s_xor_b32 s50, s50, s25
	s_sub_i32 s25, s50, s25
	s_lshl_b32 s50, s25, 7
	s_mul_i32 s25, s25, s24
	s_sub_i32 s1, s1, s25
	v_or_b32_e32 v2, s50, v130
	s_ashr_i32 s24, s50, 31
	s_lshl_b32 s1, s1, 8
	s_mul_i32 s25, s80, s24
	v_mul_lo_u32 v4, s81, v2
	v_mad_u64_u32 v[2:3], s[50:51], s80, v2, 0
	s_add_i32 s24, s1, s33
	v_add3_u32 v3, v3, s25, v4
	v_lshl_add_u64 v[2:3], v[2:3], 2, s[78:79]
	s_ashr_i32 s25, s24, 31
	v_lshl_add_u64 v[2:3], s[24:25], 2, v[2:3]
	v_lshl_add_u64 v[2:3], v[132:133], 2, v[2:3]
	v_lshl_add_u64 v[2:3], v[2:3], 0, v[162:163]
	s_lshl_b64 s[24:25], s[80:81], 2
	v_lshl_add_u64 v[10:11], v[2:3], 0, s[24:25]
	global_load_dwordx4 v[2:5], v[2:3], off
	s_nop 0
	global_load_dwordx4 v[6:9], v[10:11], off
	v_lshl_add_u64 v[10:11], v[10:11], 0, s[24:25]
	v_lshl_add_u64 v[18:19], v[10:11], 0, s[24:25]
	global_load_dwordx4 v[10:13], v[10:11], off
	s_nop 0
	global_load_dwordx4 v[14:17], v[18:19], off
	v_lshl_add_u64 v[18:19], v[18:19], 0, s[24:25]
	v_lshl_add_u64 v[26:27], v[18:19], 0, s[24:25]
	v_lshl_add_u64 v[30:31], v[26:27], 0, s[24:25]
	v_lshl_add_u64 v[34:35], v[30:31], 0, s[24:25]
	v_lshl_add_u64 v[38:39], v[34:35], 0, s[24:25]
	v_lshl_add_u64 v[42:43], v[38:39], 0, s[24:25]
	v_lshl_add_u64 v[54:55], v[42:43], 0, s[24:25]
	v_lshl_add_u64 v[62:63], v[54:55], 0, s[24:25]
	v_lshl_add_u64 v[70:71], v[62:63], 0, s[24:25]
	v_lshl_add_u64 v[78:79], v[70:71], 0, s[24:25]
	v_lshl_add_u64 v[90:91], v[78:79], 0, s[24:25]
	global_load_dwordx4 v[18:21], v[18:19], off
	s_nop 0
	global_load_dwordx4 v[22:25], v[26:27], off
	s_nop 0
	global_load_dwordx4 v[26:29], v[30:31], off
	s_nop 0
	global_load_dwordx4 v[30:33], v[34:35], off
	s_nop 0
	global_load_dwordx4 v[34:37], v[38:39], off
	s_nop 0
	global_load_dwordx4 v[38:41], v[42:43], off
	s_nop 0
	global_load_dwordx4 v[42:45], v[54:55], off
	s_nop 0
	global_load_dwordx4 v[54:57], v[62:63], off
	s_nop 0
	global_load_dwordx4 v[62:65], v[70:71], off
	s_nop 0
	global_load_dwordx4 v[70:73], v[78:79], off
	s_nop 0
	global_load_dwordx4 v[78:81], v[90:91], off
	v_lshl_add_u64 v[90:91], v[90:91], 0, s[24:25]
	global_load_dwordx4 v[90:93], v[90:91], off
	s_mov_b32 s98, 1

; #define GAS __attribute__((address_space(1)))
; __device__ __forceinline__ int conv_dst_row(int mode, int n) {
;     if (mode == 1) { if (n >= C_AQ && n < C_AV) { const int hb = n & ~127, dd = n & 127; return hb + (dd < 64 ? 2 * dd : 2 * (dd - 64) + 1); } return n; }
;     if (mode == 2) return (n >> 7) * 256 + (n & 127);
;     if (mode == 3) return (n >> 7) * 256 + 128 + (n & 127);
;     return n;
; }
; __device__ __forceinline__ void conv8_store(const ConvJob& J, int tid, const f32x4 (&v)[16]) {
;     const int nblk = J.ncols / 256, k0 = 128 * (J.item / nblk), n0 = J.ncol0 + 256 * (J.item % nblk);
;     const int lane = tid & 63, w = tid >> 6, kg = lane & 7, nq = lane >> 3; const float sc8 = J.sc8;
; #pragma unroll
;     for (int c = 0; c < 4; ++c) { u32x4 o;
; #pragma unroll
;         for (int d = 0; d < 4; ++d) { int wv = __builtin_amdgcn_cvt_pk_fp8_f32(v[4 * d][c] * sc8, v[4 * d + 1][c] * sc8, 0, false);
;             wv = __builtin_amdgcn_cvt_pk_fp8_f32(v[4 * d + 2][c] * sc8, v[4 * d + 3][c] * sc8, wv, true); o[d] = (unsigned)wv; }
;         *(GAS u32x4*)(J.WT + (size_t)conv_dst_row(J.mode, n0 - J.ncol0 + 32 * w + 4 * nq + c) * J.K + k0 + 16 * kg) = o; }
.LBB0_564:
	s_cmp_lg_u32 s98, 0
	s_cbranch_scc1 .Lcvw_b
	s_waitcnt vmcnt(0)
.Lcvw_b:
	s_waitcnt vmcnt(16)
	v_mul_f32_e32 v141, s24, v46
	v_mul_f32_e32 v143, s24, v50
	v_mov_b32_e32 v142, v163
	v_cvt_pk_fp8_f32 v142, v141, v143
	v_mul_f32_e32 v145, s24, v74
	v_mul_f32_e32 v146, s24, v82
	v_mov_b32_e32 v143, v163
	v_cvt_pk_fp8_f32 v143, v145, v146
	v_mul_f32_e32 v141, s24, v58
	v_mul_f32_e32 v144, s24, v66
	v_cvt_pk_fp8_f32 v142, v141, v144 op_sel:[0,0,1]
	v_mul_f32_e32 v141, s24, v86
	v_mul_f32_e32 v144, s24, v94
	v_cvt_pk_fp8_f32 v143, v141, v144 op_sel:[0,0,1]
	v_mul_f32_e32 v141, s24, v98
	v_mul_f32_e32 v145, s24, v102
	v_mov_b32_e32 v144, v163
	v_cvt_pk_fp8_f32 v144, v141, v145
	v_mul_f32_e32 v147, s24, v114
	v_mul_f32_e32 v148, s24, v118
	v_mov_b32_e32 v145, v163
	v_cvt_pk_fp8_f32 v145, v147, v148
	v_mul_f32_e32 v141, s24, v106
	v_mul_f32_e32 v146, s24, v110
	v_cvt_pk_fp8_f32 v144, v141, v146 op_sel:[0,0,1]
	v_mul_f32_e32 v141, s24, v122
	v_mul_f32_e32 v146, s24, v126
	v_cvt_pk_fp8_f32 v145, v141, v146 op_sel:[0,0,1]
	v_ashrrev_i32_e32 v141, 31, v140
	v_mov_b64_e32 v[146:147], s[80:81]
	s_lshl_b32 s82, s51, 7
	v_mad_u64_u32 v[146:147], s[50:51], s78, v140, v[146:147]
	v_mul_lo_u32 v140, s79, v140
	v_mul_lo_u32 v141, s78, v141
	s_ashr_i32 s83, s82, 31
	v_add3_u32 v147, v140, v147, v141
	s_add_i32 s33, s33, s25
	v_lshl_add_u64 v[140:141], v[146:147], 0, s[82:83]
	v_add_u32_e32 v139, s33, v135
	v_lshl_add_u64 v[140:141], v[140:141], 0, v[130:131]
	global_store_dwordx4 v[140:141], v[142:145], off
	s_cmp_lt_i32 s1, 2
	s_mov_b64 s[84:85], -1
	v_or_b32_e32 v142, 1, v139
	v_subrev_u32_e32 v141, s25, v142
	s_cbranch_scc1 .LBB0_570
	s_cmp_gt_i32 s1, 2
	v_lshlrev_b32_e32 v143, 1, v141
	s_cbranch_scc0 .LBB0_567
	v_and_b32_e32 v140, 0xffffff00, v143
	v_and_b32_e32 v144, 0x7d, v142
	v_or3_b32 v140, v144, v140, s2
	s_mov_b64 s[84:85], 0
